# idle-slot weight conversion: each idle workgroup reserves its whole quota with one atomic on the queue head instead of one atomic per tile
# speedup vs baseline: 1.0091x; 1.0027x over previous
; #define SEAM(k) do { if (IN(k) && IN((k) + 1)) xcd_barrier(bar); \
;         if (PROBE_MASK) { const unsigned long long t_ = __builtin_amdgcn_s_memrealtime(); if ((PROBE_MASK >> (k)) & 1u) pr_acc += t_ - pr_t0; pr_t0 = t_; } } while (0)
; __device__ __forceinline__ void convert_deferred(const Ptrs& P, unsigned char* lds, int quota) {
;     const int tid = threadIdx.x, wid = tid >> 6, lane = tid & 63;
;     float* tile = (float*)lds;
;     volatile __attribute__((address_space(3))) int* slot = (volatile __attribute__((address_space(3))) int*)((__attribute__((address_space(3))) unsigned char*)lds + 131072 + 320 + 11000);
;     unsigned* q = (unsigned*)(P.ws + WS_CTL) + CW_DEFQ;
;     for (int n = 0; n < quota; ++n) {
;         __syncthreads();
;         if (tid == 0) *slot = (int)atomicAdd(q, 1u);
;         __syncthreads();
;         const int t = *slot;
;         if (t >= DEF_GU + DEF_DN) break;
;         const bool gu = t < DEF_GU;
;         const float* src = gu ? P.in[34] : P.in[36]; bf16* dst = (bf16*)(P.ws + (gu ? WS_WGU : WS_WDN));
;         const int N = gu ? 2048 : 1024, ntn = N / 256, it = gu ? 2 * NE * 16 * 8 - DEF_GU + t : 2 * NE * 16 * 4 - DEF_DN + (t - DEF_GU);
; __global__ void __launch_bounds__(NT, 2) mega(Args args) {
;     ...
;         if (IDLE_LAST(68 * 7)) convert_deferred(P, lds, 4); } SEAM(2);
.LBB0_779:
	s_abs_i32 s3, s62
	v_cvt_f32_u32_e32 v2, s3
	s_sub_i32 s4, 0, s3
	s_mov_b32 s5, 0
	v_rcp_iflag_f32_e32 v2, v2
	s_nop 0
	v_mul_f32_e32 v2, 0x4f7ffffe, v2
	v_cvt_u32_f32_e32 v2, v2
	s_nop 0
	v_readfirstlane_b32 s6, v2
	s_mul_i32 s4, s4, s6
	s_mul_hi_u32 s4, s6, s4
	s_add_i32 s6, s6, s4
	s_mul_hi_u32 s4, s6, 0x1dc
	s_mul_i32 s4, s4, s3
	s_sub_i32 s4, 0x1dc, s4
	s_sub_i32 s6, s4, s3
	s_cmp_ge_u32 s4, s3
	s_cselect_b32 s4, s6, s4
	s_sub_i32 s6, s4, s3
	s_cmp_ge_u32 s4, s3
	s_cselect_b32 s3, s6, s4
	s_cmp_eq_u32 s3, 0
	s_cselect_b64 s[6:7], -1, 0
	s_cmp_lt_i32 s2, s3
	s_cselect_b64 s[8:9], -1, 0
	s_or_b64 s[6:7], s[6:7], s[8:9]
	s_and_b64 vcc, exec, s[6:7]
	s_cbranch_vccnz .LBB0_789
	v_and_b32_e32 v2, 0x7c, v155
	v_lshlrev_b32_e32 v3, 5, v0
	s_movk_i32 s3, 0x400
	v_lshrrev_b32_e32 v4, 6, v0
	v_and_or_b32 v12, v3, s3, v2
	v_bfe_u32 v2, v0, 3, 3
	v_lshl_or_b32 v5, v4, 5, v2
	v_lshlrev_b32_e32 v2, 3, v0
	v_lshl_add_u32 v11, v182, 4, 0
	v_and_b32_e32 v2, 56, v2
	v_mul_u32_u24_e32 v16, 0x2020, v4
	v_mov_b32_e32 v3, 0
	v_lshl_add_u32 v27, v5, 2, 0
	v_mul_u32_u24_e32 v28, 0x404, v2
	v_lshlrev_b32_e32 v10, 6, v5
	s_add_i32 s12, 0, 0x22c38
	v_add_u32_e32 v16, v11, v16
	v_and_b32_e32 v13, 0xfc, v155
	v_and_b32_e32 v14, 56, v154
	s_mov_b32 s3, 6
	s_mov_b32 s91, 0
	v_or_b32_e32 v4, 0x200, v10
	v_mov_b32_e32 v5, v3
	v_or_b32_e32 v6, 0x400, v10
	v_mov_b32_e32 v7, v3
	v_or_b32_e32 v8, 0x600, v10
	v_mov_b32_e32 v9, v3
	v_mov_b32_e32 v15, s12
	s_movk_i32 s13, 0x13eb
	s_movk_i32 s14, 0x800
	s_mov_b32 s15, 0x1104e000
	s_movk_i32 s16, -1004
	v_add_u32_e32 v17, 0x404, v16
	v_add_u32_e32 v18, 0x40c, v16
	v_add_u32_e32 v19, 0x808, v16
	v_add_u32_e32 v20, 0xc0c, v16
	v_add_u32_e32 v21, 0xc14, v16
	v_add_u32_e32 v22, 0x1414, v16
	v_add_u32_e32 v23, 0x141c, v16
	v_add_u32_e32 v24, 0x1818, v16
	v_add_u32_e32 v25, 0x1c1c, v16
	v_add_u32_e32 v26, 0x1c24, v16
	v_lshlrev_b32_e32 v2, 1, v2
	v_add_u32_e32 v27, v27, v28
	v_lshlrev_b32_e32 v10, 1, v10
	s_branch .LBB0_782

; __device__ __forceinline__ void convert_deferred(const Ptrs& P, unsigned char* lds, int quota) {
;     ...
;     for (int n = 0; n < quota; ++n) {
;         __syncthreads();
;         if (tid == 0) *slot = (int)atomicAdd(q, 1u);
;         __syncthreads();
;         const int t = *slot;
.LBB0_782:
	s_waitcnt vmcnt(0) lgkmcnt(0)
	s_barrier
	s_mov_b64 s[6:7], exec
	v_readlane_b32 s8, v254, 22
	v_readlane_b32 s9, v254, 23
	s_and_b64 s[8:9], s[6:7], s[8:9]
	s_mov_b64 exec, s[8:9]
	s_cbranch_execz .LBB0_786
	s_mov_b64 s[10:11], exec
	v_mbcnt_lo_u32_b32 v11, s10, 0
	v_mbcnt_hi_u32_b32 v11, s11, v11
	v_cmp_eq_u32_e32 vcc, 0, v11
	s_and_saveexec_b64 s[8:9], vcc
	s_cbranch_execz .LBB0_785
	s_cmp_lg_u32 s91, 0
	s_cbranch_scc1 .Lpop0_have
	v_mov_b32_e32 v28, s3
	global_atomic_add v28, v3, v28, s[78:79] offset:1024 sc0
	s_waitcnt vmcnt(0)
	v_readfirstlane_b32 s90, v28
	s_mov_b32 s91, 1
	s_nop 1
.Lpop0_have:
	v_mov_b32_e32 v28, s90
	s_add_i32 s90, s90, 1

; #define SEAM(k) do { if (IN(k) && IN((k) + 1)) xcd_barrier(bar); \
;         if (PROBE_MASK) { const unsigned long long t_ = __builtin_amdgcn_s_memrealtime(); if ((PROBE_MASK >> (k)) & 1u) pr_acc += t_ - pr_t0; pr_t0 = t_; } } while (0)
; __device__ __forceinline__ void convert_deferred(const Ptrs& P, unsigned char* lds, int quota) {
;     const int tid = threadIdx.x, wid = tid >> 6, lane = tid & 63;
;     float* tile = (float*)lds;
;     volatile __attribute__((address_space(3))) int* slot = (volatile __attribute__((address_space(3))) int*)((__attribute__((address_space(3))) unsigned char*)lds + 131072 + 320 + 11000);
;     unsigned* q = (unsigned*)(P.ws + WS_CTL) + CW_DEFQ;
;     for (int n = 0; n < quota; ++n) {
;         __syncthreads();
;         if (tid == 0) *slot = (int)atomicAdd(q, 1u);
;         __syncthreads();
;         const int t = *slot;
;         if (t >= DEF_GU + DEF_DN) break;
;         const bool gu = t < DEF_GU;
;         const float* src = gu ? P.in[34] : P.in[36]; bf16* dst = (bf16*)(P.ws + (gu ? WS_WGU : WS_WDN));
;         const int N = gu ? 2048 : 1024, ntn = N / 256, it = gu ? 2 * NE * 16 * 8 - DEF_GU + t : 2 * NE * 16 * 4 - DEF_DN + (t - DEF_GU);
; __global__ void __launch_bounds__(NT, 2) mega(Args args) {
;     ...
;         if (IDLE_LAST(68 * 4)) convert_deferred(P, lds, 4); } SEAM(6);
.LBB0_1286:
	s_abs_i32 s3, s62
	v_cvt_f32_u32_e32 v2, s3
	s_sub_i32 s4, 0, s3
	s_mov_b32 s5, 0
	v_rcp_iflag_f32_e32 v2, v2
	s_nop 0
	v_mul_f32_e32 v2, 0x4f7ffffe, v2
	v_cvt_u32_f32_e32 v2, v2
	s_nop 0
	v_readfirstlane_b32 s6, v2
	s_mul_i32 s4, s4, s6
	s_mul_hi_u32 s4, s6, s4
	s_add_i32 s6, s6, s4
	s_mul_hi_u32 s4, s6, 0x110
	s_mul_i32 s4, s4, s3
	s_sub_i32 s4, 0x110, s4
	s_sub_i32 s6, s4, s3
	s_cmp_ge_u32 s4, s3
	s_cselect_b32 s4, s6, s4
	s_sub_i32 s6, s4, s3
	s_cmp_ge_u32 s4, s3
	s_cselect_b32 s3, s6, s4
	s_cmp_eq_u32 s3, 0
	s_cselect_b64 s[6:7], -1, 0
	s_cmp_lt_i32 s2, s3
	s_cselect_b64 s[8:9], -1, 0
	s_or_b64 s[6:7], s[6:7], s[8:9]
	s_and_b64 vcc, exec, s[6:7]
	s_cbranch_vccnz .LBB0_1296
	v_and_b32_e32 v2, 0x7c, v188
	v_lshlrev_b32_e32 v3, 5, v0
	s_movk_i32 s3, 0x400
	v_and_or_b32 v12, v3, s3, v2
	v_bfe_u32 v2, v0, 3, 3
	v_lshl_or_b32 v4, v1, 5, v2
	v_lshlrev_b32_e32 v2, 3, v0
	v_lshl_add_u32 v11, v182, 4, 0
	v_and_b32_e32 v2, 56, v2
	v_mul_u32_u24_e32 v16, 0x2020, v1
	v_mov_b32_e32 v3, 0
	v_lshl_add_u32 v27, v4, 2, 0
	v_mul_u32_u24_e32 v28, 0x404, v2
	v_lshlrev_b32_e32 v10, 6, v4
	s_add_i32 s12, 0, 0x22c38
	v_add_u32_e32 v16, v11, v16
	v_and_b32_e32 v13, 0xfc, v188
	v_and_b32_e32 v14, 56, v185
	s_mov_b32 s3, 9
	s_mov_b32 s91, 0
	v_or_b32_e32 v4, 0x200, v10
	v_mov_b32_e32 v5, v3
	v_or_b32_e32 v6, 0x400, v10
	v_mov_b32_e32 v7, v3
	v_or_b32_e32 v8, 0x600, v10
	v_mov_b32_e32 v9, v3
	v_mov_b32_e32 v15, s12
	s_movk_i32 s13, 0x13eb
	s_movk_i32 s14, 0x800
	s_mov_b32 s15, 0x1104e000
	s_movk_i32 s16, -1004
	v_add_u32_e32 v17, 0x404, v16
	v_add_u32_e32 v18, 0x40c, v16
	v_add_u32_e32 v19, 0x808, v16
	v_add_u32_e32 v20, 0xc0c, v16
	v_add_u32_e32 v21, 0xc14, v16
	v_add_u32_e32 v22, 0x1414, v16
	v_add_u32_e32 v23, 0x141c, v16
	v_add_u32_e32 v24, 0x1818, v16
	v_add_u32_e32 v25, 0x1c1c, v16
	v_add_u32_e32 v26, 0x1c24, v16
	v_lshlrev_b32_e32 v2, 1, v2
	v_add_u32_e32 v27, v27, v28
	v_lshlrev_b32_e32 v10, 1, v10
	s_branch .LBB0_1289

; #define LAS __attribute__((address_space(3)))
; #define SEAM(k) do { if (IN(k) && IN((k) + 1)) xcd_barrier(bar); \
;         if (PROBE_MASK) { const unsigned long long t_ = __builtin_amdgcn_s_memrealtime(); if ((PROBE_MASK >> (k)) & 1u) pr_acc += t_ - pr_t0; pr_t0 = t_; } } while (0)
; __device__ __forceinline__ void convert_deferred(const Ptrs& P, unsigned char* lds, int quota) {
;     const int tid = threadIdx.x, wid = tid >> 6, lane = tid & 63;
;     float* tile = (float*)lds;
;     volatile __attribute__((address_space(3))) int* slot = (volatile __attribute__((address_space(3))) int*)((__attribute__((address_space(3))) unsigned char*)lds + 131072 + 320 + 11000);
;     unsigned* q = (unsigned*)(P.ws + WS_CTL) + CW_DEFQ;
;     for (int n = 0; n < quota; ++n) {
;         __syncthreads();
;         if (tid == 0) *slot = (int)atomicAdd(q, 1u);
;         __syncthreads();
;         const int t = *slot;
;         if (t >= DEF_GU + DEF_DN) break;
;         const bool gu = t < DEF_GU;
;         const float* src = gu ? P.in[34] : P.in[36]; bf16* dst = (bf16*)(P.ws + (gu ? WS_WGU : WS_WDN));
;         const int N = gu ? 2048 : 1024, ntn = N / 256, it = gu ? 2 * NE * 16 * 8 - DEF_GU + t : 2 * NE * 16 * 4 - DEF_DN + (t - DEF_GU);
; __global__ void __launch_bounds__(NT, 2) mega(Args args) {
;     ...
;         { const int rem_ = ((LAS int*)(LDSP + MISC_OFF + 256))[96] % G; if (rem_ != 0 && vcu >= rem_) convert_deferred(P, lds, 5); } } SEAM(9);
.LBB0_1609:
	s_abs_i32 s0, s62
	v_cvt_f32_u32_e32 v2, s0
	s_sub_i32 s5, 0, s0
	s_abs_i32 s4, s9
	s_ashr_i32 s3, s9, 31
	v_rcp_iflag_f32_e32 v2, v2
	s_mov_b32 s1, 0
	v_mul_f32_e32 v2, 0x4f7ffffe, v2
	v_cvt_u32_f32_e32 v2, v2
	s_nop 0
	v_readfirstlane_b32 s6, v2
	s_mul_i32 s5, s5, s6
	s_mul_hi_u32 s5, s6, s5
	s_add_i32 s6, s6, s5
	s_mul_hi_u32 s5, s4, s6
	s_mul_i32 s5, s5, s0
	s_sub_i32 s4, s4, s5
	s_sub_i32 s5, s4, s0
	s_cmp_ge_u32 s4, s0
	s_cselect_b32 s4, s5, s4
	s_sub_i32 s5, s4, s0
	s_cmp_ge_u32 s4, s0
	s_cselect_b32 s0, s5, s4
	s_xor_b32 s0, s0, s3
	s_sub_i32 s0, s0, s3
	s_cmp_eq_u32 s0, 0
	v_readlane_b32 s3, v254, 2
	s_cselect_b64 s[4:5], -1, 0
	s_cmp_lt_i32 s3, s0
	s_cselect_b64 s[6:7], -1, 0
	s_or_b64 s[4:5], s[4:5], s[6:7]
	s_and_b64 vcc, exec, s[4:5]
	s_cbranch_vccnz .LBB0_1619
	v_and_b32_e32 v2, 0x7c, v175
	v_lshlrev_b32_e32 v3, 5, v0
	s_movk_i32 s0, 0x400
	v_and_or_b32 v12, v3, s0, v2
	v_bfe_u32 v2, v0, 3, 3
	v_lshl_or_b32 v4, v1, 5, v2
	v_lshlrev_b32_e32 v2, 3, v0
	v_lshl_add_u32 v11, v182, 4, 0
	v_and_b32_e32 v2, 56, v2
	v_mul_u32_u24_e32 v16, 0x2020, v1
	v_mov_b32_e32 v3, 0
	v_lshl_add_u32 v27, v4, 2, 0
	v_mul_u32_u24_e32 v28, 0x404, v2
	v_lshlrev_b32_e32 v10, 6, v4
	s_add_i32 s10, 0, 0x22c38
	v_add_u32_e32 v16, v11, v16
	s_mov_b32 s3, 8
	s_mov_b32 s91, 0
	v_and_b32_e32 v13, 0xfc, v175
	v_and_b32_e32 v14, 56, v173
	v_or_b32_e32 v4, 0x200, v10
	v_mov_b32_e32 v5, v3
	v_or_b32_e32 v6, 0x400, v10
	v_mov_b32_e32 v7, v3
	v_or_b32_e32 v8, 0x600, v10
	v_mov_b32_e32 v9, v3
	v_mov_b32_e32 v15, s10
	s_movk_i32 s11, 0x13eb
	s_movk_i32 s12, 0x800
	s_mov_b32 s13, 0x1104e000
	s_movk_i32 s14, -1004
	v_add_u32_e32 v17, 0x404, v16
	v_add_u32_e32 v18, 0x40c, v16
	v_add_u32_e32 v19, 0x808, v16
	v_add_u32_e32 v20, 0xc0c, v16
	v_add_u32_e32 v21, 0xc14, v16
	v_add_u32_e32 v22, 0x1414, v16
	v_add_u32_e32 v23, 0x141c, v16
	v_add_u32_e32 v24, 0x1818, v16
	v_add_u32_e32 v25, 0x1c1c, v16
	v_add_u32_e32 v26, 0x1c24, v16
	v_lshlrev_b32_e32 v2, 1, v2
	v_add_u32_e32 v27, v27, v28
	v_lshlrev_b32_e32 v10, 1, v10
	s_branch .LBB0_1612

; __device__ __forceinline__ void convert_deferred(const Ptrs& P, unsigned char* lds, int quota) {
;     ...
;     for (int n = 0; n < quota; ++n) {
;         __syncthreads();
;         if (tid == 0) *slot = (int)atomicAdd(q, 1u);
;         __syncthreads();
;         const int t = *slot;
.LBB0_1612:
	s_waitcnt vmcnt(0)
	s_barrier
	s_mov_b64 s[4:5], exec
	v_readlane_b32 s6, v254, 22
	v_readlane_b32 s7, v254, 23
	s_and_b64 s[6:7], s[4:5], s[6:7]
	s_mov_b64 exec, s[6:7]
	s_cbranch_execz .LBB0_1616
	s_mov_b64 s[8:9], exec
	v_mbcnt_lo_u32_b32 v11, s8, 0
	v_mbcnt_hi_u32_b32 v11, s9, v11
	v_cmp_eq_u32_e32 vcc, 0, v11
	s_and_saveexec_b64 s[6:7], vcc
	s_cbranch_execz .LBB0_1615
	s_cmp_lg_u32 s91, 0
	s_cbranch_scc1 .Lpop2_have
	v_mov_b32_e32 v28, s3
	global_atomic_add v28, v3, v28, s[78:79] offset:1024 sc0
	s_waitcnt vmcnt(0)
	v_readfirstlane_b32 s90, v28
	s_mov_b32 s91, 1
	s_nop 1

; #define SEAM(k) do { if (IN(k) && IN((k) + 1)) xcd_barrier(bar); \
;         if (PROBE_MASK) { const unsigned long long t_ = __builtin_amdgcn_s_memrealtime(); if ((PROBE_MASK >> (k)) & 1u) pr_acc += t_ - pr_t0; pr_t0 = t_; } } while (0)
; __device__ __forceinline__ void convert_deferred(const Ptrs& P, unsigned char* lds, int quota) {
;     const int tid = threadIdx.x, wid = tid >> 6, lane = tid & 63;
;     float* tile = (float*)lds;
;     volatile __attribute__((address_space(3))) int* slot = (volatile __attribute__((address_space(3))) int*)((__attribute__((address_space(3))) unsigned char*)lds + 131072 + 320 + 11000);
;     unsigned* q = (unsigned*)(P.ws + WS_CTL) + CW_DEFQ;
;     for (int n = 0; n < quota; ++n) {
;         __syncthreads();
;         if (tid == 0) *slot = (int)atomicAdd(q, 1u);
;         __syncthreads();
;         const int t = *slot;
;         if (t >= DEF_GU + DEF_DN) break;
;         const bool gu = t < DEF_GU;
;         const float* src = gu ? P.in[34] : P.in[36]; bf16* dst = (bf16*)(P.ws + (gu ? WS_WGU : WS_WDN));
;         const int N = gu ? 2048 : 1024, ntn = N / 256, it = gu ? 2 * NE * 16 * 8 - DEF_GU + t : 2 * NE * 16 * 4 - DEF_DN + (t - DEF_GU);
; __global__ void __launch_bounds__(NT, 2) mega(Args args) {
;     ...
;         if (IDLE_LAST(68 * 12)) convert_deferred(P, lds, 4); } SEAM(11);
.LBB0_1851:
	s_abs_i32 s0, s62
	v_cvt_f32_u32_e32 v2, s0
	s_sub_i32 s3, 0, s0
	v_readlane_b32 s56, v254, 40
	s_mov_b32 s1, 0
	v_rcp_iflag_f32_e32 v2, v2
	v_readlane_b32 s57, v254, 41
	v_mul_f32_e32 v2, 0x4f7ffffe, v2
	v_cvt_u32_f32_e32 v2, v2
	s_nop 0
	v_readfirstlane_b32 s4, v2
	s_mul_i32 s3, s3, s4
	s_mul_hi_u32 s3, s4, s3
	s_add_i32 s4, s4, s3
	s_mul_hi_u32 s3, s4, 0x330
	s_mul_i32 s3, s3, s0
	s_sub_i32 s3, 0x330, s3
	s_sub_i32 s4, s3, s0
	s_cmp_ge_u32 s3, s0
	s_cselect_b32 s3, s4, s3
	s_sub_i32 s4, s3, s0
	s_cmp_ge_u32 s3, s0
	s_cselect_b32 s0, s4, s3
	s_cmp_eq_u32 s0, 0
	s_cselect_b64 s[4:5], -1, 0
	s_cmp_lt_i32 s2, s0
	s_cselect_b64 s[6:7], -1, 0
	s_or_b64 s[4:5], s[4:5], s[6:7]
	s_and_b64 vcc, exec, s[4:5]
	s_cbranch_vccnz .LBB0_1861
	v_and_b32_e32 v2, 0x7c, v218
	v_lshlrev_b32_e32 v3, 5, v0
	s_movk_i32 s0, 0x400
	v_and_or_b32 v12, v3, s0, v2
	v_bfe_u32 v2, v0, 3, 3
	v_lshl_or_b32 v4, v1, 5, v2
	v_lshlrev_b32_e32 v2, 3, v0
	v_lshl_add_u32 v11, v182, 4, 0
	v_and_b32_e32 v2, 56, v2
	v_mul_u32_u24_e32 v16, 0x2020, v1
	v_mov_b32_e32 v3, 0
	s_waitcnt vmcnt(0)
	v_lshl_add_u32 v27, v4, 2, 0
	v_mul_u32_u24_e32 v28, 0x404, v2
	v_lshlrev_b32_e32 v10, 6, v4
	s_add_i32 s10, 0, 0x22c38
	v_add_u32_e32 v16, v11, v16
	v_and_b32_e32 v13, 0xfc, v218
	v_and_b32_e32 v14, 56, v179
	s_mov_b32 s3, 10
	s_mov_b32 s91, 0
	v_or_b32_e32 v4, 0x200, v10
	v_mov_b32_e32 v5, v3
	v_or_b32_e32 v6, 0x400, v10
	v_mov_b32_e32 v7, v3
	v_or_b32_e32 v8, 0x600, v10
	v_mov_b32_e32 v9, v3
	v_mov_b32_e32 v15, s10
	s_movk_i32 s11, 0x13eb
	s_movk_i32 s12, 0x800
	s_mov_b32 s13, 0x1104e000
	s_movk_i32 s14, -1004
	v_add_u32_e32 v17, 0x404, v16
	v_add_u32_e32 v18, 0x40c, v16
	v_add_u32_e32 v19, 0x808, v16
	v_add_u32_e32 v20, 0xc0c, v16
	v_add_u32_e32 v21, 0xc14, v16
	v_add_u32_e32 v22, 0x1414, v16
	v_add_u32_e32 v23, 0x141c, v16
	v_add_u32_e32 v24, 0x1818, v16
	v_add_u32_e32 v25, 0x1c1c, v16
	v_add_u32_e32 v26, 0x1c24, v16
	v_lshlrev_b32_e32 v2, 1, v2
	v_add_u32_e32 v27, v27, v28
	v_lshlrev_b32_e32 v10, 1, v10
	s_branch .LBB0_1854

; __device__ __forceinline__ void convert_deferred(const Ptrs& P, unsigned char* lds, int quota) {
;     ...
;     for (int n = 0; n < quota; ++n) {
;         __syncthreads();
;         if (tid == 0) *slot = (int)atomicAdd(q, 1u);
;         __syncthreads();
;         const int t = *slot;
.LBB0_1854:
	s_waitcnt lgkmcnt(0)
	s_barrier
	s_mov_b64 s[4:5], exec
	v_readlane_b32 s6, v254, 22
	v_readlane_b32 s7, v254, 23
	s_and_b64 s[6:7], s[4:5], s[6:7]
	s_mov_b64 exec, s[6:7]
	s_cbranch_execz .LBB0_1858
	s_mov_b64 s[8:9], exec
	v_mbcnt_lo_u32_b32 v11, s8, 0
	v_mbcnt_hi_u32_b32 v11, s9, v11
	v_cmp_eq_u32_e32 vcc, 0, v11
	s_and_saveexec_b64 s[6:7], vcc
	s_cbranch_execz .LBB0_1857
	s_cmp_lg_u32 s91, 0
	s_cbranch_scc1 .Lpop3_have
	v_mov_b32_e32 v28, s3
	global_atomic_add v28, v3, v28, s[78:79] offset:1024 sc0
	s_waitcnt vmcnt(0)
	v_readfirstlane_b32 s90, v28
	s_mov_b32 s91, 1
	s_nop 1
